# partial-sum write issued right after the W2 dot; bias patch and loop bookkeeping behind it, noise reads earlier
# speedup vs baseline: 1.0226x; 1.0046x over previous
.LBB1_4:
	s_and_saveexec_b64 s[8:9], s[2:3]
	v_perm_b32 v5, v1, v102, s23
	v_perm_b32 v9, v121, v103, s23
	v_perm_b32 v17, v144, v115, s23
	v_perm_b32 v29, v145, v116, s23
	s_or_b64 exec, exec, s[8:9]
	v_mfma_f32_16x16x32_f16 v[164:167], v[30:33], v[2:5], 0
	v_mfma_f32_16x16x32_f16 v[180:183], v[22:25], v[2:5], 0
	s_cmp_lg_u32 s22, 0x818000
	v_mfma_f32_16x16x32_f16 v[168:171], v[30:33], v[6:9], 0
	v_mfma_f32_16x16x32_f16 v[184:187], v[22:25], v[6:9], 0
	s_cselect_b32 s9, s11, 15
	v_mfma_f32_16x16x32_f16 v[172:175], v[30:33], v[14:17], 0
	v_mfma_f32_16x16x32_f16 v[188:191], v[22:25], v[14:17], 0
	v_mfma_f32_16x16x32_f16 v[176:179], v[30:33], v[26:29], 0
	v_mfma_f32_16x16x32_f16 v[192:195], v[22:25], v[26:29], 0
	v_mfma_f32_16x16x32_f16 v[196:199], v[18:21], v[2:5], 0
	v_cvt_pk_f16_f32 v122, v164, v165
	v_cvt_pk_f16_f32 v123, v166, v167
	v_pk_max_f16 v122, v122, 0
	v_pk_max_f16 v123, v123, 0
	v_cvt_pk_f16_f32 v124, v180, v181
	v_cvt_pk_f16_f32 v125, v182, v183
	v_pk_max_f16 v124, v124, 0
	v_pk_max_f16 v125, v125, 0
	ds_write_b128 v107, v[122:125]
	v_mfma_f32_16x16x32_f16 v[212:215], v[10:13], v[2:5], 0
	v_cvt_pk_f16_f32 v126, v168, v169
	v_cvt_pk_f16_f32 v127, v170, v171
	v_pk_max_f16 v126, v126, 0
	v_pk_max_f16 v127, v127, 0
	v_cvt_pk_f16_f32 v128, v184, v185
	v_cvt_pk_f16_f32 v129, v186, v187
	v_pk_max_f16 v128, v128, 0
	v_pk_max_f16 v129, v129, 0
	ds_write_b128 v107, v[126:129] offset:16384
	v_mfma_f32_16x16x32_f16 v[200:203], v[18:21], v[6:9], 0
	v_cvt_pk_f16_f32 v134, v172, v173
	v_cvt_pk_f16_f32 v135, v174, v175
	v_pk_max_f16 v134, v134, 0
	v_pk_max_f16 v135, v135, 0
	v_cvt_pk_f16_f32 v136, v188, v189
	v_cvt_pk_f16_f32 v137, v190, v191
	v_pk_max_f16 v136, v136, 0
	v_pk_max_f16 v137, v137, 0
	ds_write_b128 v107, v[134:137] offset:32768
	v_mfma_f32_16x16x32_f16 v[216:219], v[10:13], v[6:9], 0
	v_cvt_pk_f16_f32 v138, v176, v177
	v_cvt_pk_f16_f32 v139, v178, v179
	v_pk_max_f16 v138, v138, 0
	v_pk_max_f16 v139, v139, 0
	v_cvt_pk_f16_f32 v140, v192, v193
	v_cvt_pk_f16_f32 v141, v194, v195
	v_pk_max_f16 v140, v140, 0
	v_pk_max_f16 v141, v141, 0
	ds_write_b128 v107, v[138:141] offset:49152
	v_mfma_f32_16x16x32_f16 v[204:207], v[18:21], v[14:17], 0
	v_cvt_pk_f16_f32 v142, v196, v197
	v_cvt_pk_f16_f32 v143, v198, v199
	v_pk_max_f16 v142, v142, 0
	v_pk_max_f16 v143, v143, 0
	v_cvt_pk_f16_f32 v144, v212, v213
	v_cvt_pk_f16_f32 v145, v214, v215
	v_pk_max_f16 v144, v144, 0
	v_pk_max_f16 v145, v145, 0
	ds_write_b128 v108, v[142:145]
	v_mfma_f32_16x16x32_f16 v[220:223], v[10:13], v[14:17], 0
	v_cvt_pk_f16_f32 v152, v200, v201
	v_cvt_pk_f16_f32 v153, v202, v203
	v_pk_max_f16 v152, v152, 0
	v_pk_max_f16 v153, v153, 0
	v_cvt_pk_f16_f32 v154, v216, v217
	v_cvt_pk_f16_f32 v155, v218, v219
	v_pk_max_f16 v154, v154, 0
	v_pk_max_f16 v155, v155, 0
	ds_write_b128 v108, v[152:155] offset:16384
	v_mfma_f32_16x16x32_f16 v[208:211], v[18:21], v[26:29], 0
	v_mfma_f32_16x16x32_f16 v[224:227], v[10:13], v[26:29], 0
	v_cvt_pk_f16_f32 v156, v204, v205
	v_cvt_pk_f16_f32 v157, v206, v207
	v_pk_max_f16 v156, v156, 0
	v_pk_max_f16 v157, v157, 0
	v_cvt_pk_f16_f32 v158, v220, v221
	v_cvt_pk_f16_f32 v159, v222, v223
	v_pk_max_f16 v158, v158, 0
	v_pk_max_f16 v159, v159, 0
	ds_write_b128 v108, v[156:159] offset:32768
	v_cvt_pk_f16_f32 v160, v208, v209
	v_cvt_pk_f16_f32 v161, v210, v211
	v_pk_max_f16 v160, v160, 0
	v_pk_max_f16 v161, v161, 0
	v_cvt_pk_f16_f32 v162, v224, v225
	v_cvt_pk_f16_f32 v163, v226, v227
	v_pk_max_f16 v162, v162, 0
	v_pk_max_f16 v163, v163, 0
	ds_write_b128 v108, v[160:163] offset:49152
	v_add_u32_e32 v111, s64, v111
	v_add_u32_e32 v98, s65, v98
	s_lshl_b32 s20, s9, 7
	v_lshl_add_u64 v[0:1], s[20:21], 3, v[132:133]
	s_add_i32 s25, s22, s34
	s_lshl_b32 s8, s9, 8
	buffer_load_dwordx4 v[192:195], v147, s[16:19], s25 offen
	buffer_load_dwordx4 v[196:199], v148, s[16:19], s25 offen
	buffer_load_dwordx4 v[200:203], v149, s[16:19], s25 offen
	buffer_load_dwordx4 v[204:207], v150, s[16:19], s25 offen
	s_waitcnt vmcnt(19)
	v_mfma_f32_16x16x32_f16 v[164:167], v[58:61], v[122:125], v[240:243]
	v_mfma_f32_16x16x32_f16 v[168:171], v[58:61], v[126:129], v[240:243]
	v_mfma_f32_16x16x32_f16 v[172:175], v[58:61], v[134:137], v[240:243]
	v_mfma_f32_16x16x32_f16 v[10:13], v[58:61], v[138:141], v[240:243]
	s_waitcnt vmcnt(18)
	v_mfma_f32_16x16x32_f16 v[58:61], v[54:57], v[122:125], v[244:247]
	v_mfma_f32_16x16x32_f16 v[176:179], v[54:57], v[126:129], v[244:247]
	v_mfma_f32_16x16x32_f16 v[180:183], v[54:57], v[134:137], v[244:247]
	v_mfma_f32_16x16x32_f16 v[18:21], v[54:57], v[138:141], v[244:247]
	s_waitcnt vmcnt(17)
	v_mfma_f32_16x16x32_f16 v[54:57], v[50:53], v[122:125], v[248:251]
	v_mfma_f32_16x16x32_f16 v[184:187], v[50:53], v[126:129], v[248:251]
	v_mfma_f32_16x16x32_f16 v[188:191], v[50:53], v[134:137], v[248:251]
	v_mfma_f32_16x16x32_f16 v[22:25], v[50:53], v[138:141], v[248:251]
	s_waitcnt vmcnt(16)
	v_mfma_f32_16x16x32_f16 v[50:53], v[38:41], v[122:125], v[252:255]
	v_mfma_f32_16x16x32_f16 v[122:125], v[38:41], v[126:129], v[252:255]
	v_mfma_f32_16x16x32_f16 v[126:129], v[38:41], v[134:137], v[252:255]
	v_mfma_f32_16x16x32_f16 v[38:41], v[38:41], v[138:141], v[252:255]
	s_add_i32 s9, s22, s35
	s_waitcnt vmcnt(15)
	v_mfma_f32_16x16x32_f16 v[164:167], v[94:97], v[142:145], v[164:167]
	v_mfma_f32_16x16x32_f16 v[168:171], v[94:97], v[152:155], v[168:171]
	s_waitcnt vmcnt(14)
	v_mfma_f32_16x16x32_f16 v[58:61], v[90:93], v[142:145], v[58:61]
	v_mfma_f32_16x16x32_f16 v[176:179], v[90:93], v[152:155], v[176:179]
	s_waitcnt vmcnt(13)
	v_mfma_f32_16x16x32_f16 v[54:57], v[78:81], v[142:145], v[54:57]
	v_mfma_f32_16x16x32_f16 v[184:187], v[78:81], v[152:155], v[184:187]
	s_waitcnt vmcnt(12)
	v_mfma_f32_16x16x32_f16 v[50:53], v[34:37], v[142:145], v[50:53]
	buffer_load_dwordx4 v[140:143], v147, s[16:19], s9 offen
	buffer_load_dwordx4 v[220:223], v148, s[16:19], s9 offen
	v_mfma_f32_16x16x32_f16 v[122:125], v[34:37], v[152:155], v[122:125]
	buffer_load_dwordx4 v[152:155], v149, s[16:19], s9 offen
	buffer_load_dwordx4 v[224:227], v150, s[16:19], s9 offen
	s_mov_b32 s9, s21
	s_waitcnt lgkmcnt(0)
	s_barrier
	v_add_u32_e32 v99, s66, v99
	ds_read_b128 v[136:139], v99
	ds_read_b128 v[208:211], v99 offset:16384
	ds_read_b128 v[212:215], v99 offset:32768
	ds_read_b128 v[216:219], v99 offset:49152
	v_mfma_f32_16x16x32_f16 v[172:175], v[94:97], v[156:159], v[172:175]
	v_mfma_f32_16x16x32_f16 v[94:97], v[94:97], v[160:163], v[10:13]
	s_nop 2
	v_lshl_add_u64 v[10:11], s[8:9], 4, v[130:131]
	v_mfma_f32_16x16x32_f16 v[180:183], v[90:93], v[156:159], v[180:183]
	v_mfma_f32_16x16x32_f16 v[90:93], v[90:93], v[160:163], v[18:21]
	v_mfma_f32_16x16x32_f16 v[188:191], v[78:81], v[156:159], v[188:191]
	v_mfma_f32_16x16x32_f16 v[78:81], v[78:81], v[160:163], v[22:25]
	global_load_dwordx4 v[30:33], v[10:11], off
	s_nop 1
	global_load_dwordx4 v[22:25], v[10:11], off offset:1024
	global_load_dwordx4 v[18:21], v[10:11], off offset:2048
	s_nop 0
	global_load_dwordx4 v[10:13], v[10:11], off offset:3072
	s_nop 0
	global_load_dwordx2 v[134:135], v[0:1], off
	v_mfma_f32_16x16x32_f16 v[126:129], v[34:37], v[156:159], v[126:129]
	v_mfma_f32_16x16x32_f16 v[34:37], v[34:37], v[160:163], v[38:41]
	s_nop 2
	v_add_u32_e32 v100, s67, v100
	ds_read_b128 v[38:41], v100
	ds_read_b128 v[156:159], v100 offset:16384
	ds_read_b128 v[160:163], v100 offset:32768
	ds_read_b128 v[228:231], v100 offset:49152
	s_add_i32 s8, s22, s36
	s_waitcnt vmcnt(20) lgkmcnt(7)
	v_mfma_f32_16x16x32_f16 v[164:167], v[82:85], v[136:139], v[164:167]
	s_waitcnt lgkmcnt(6)
	v_mfma_f32_16x16x32_f16 v[168:171], v[82:85], v[208:211], v[168:171]
	s_waitcnt lgkmcnt(5)
	v_mfma_f32_16x16x32_f16 v[172:175], v[82:85], v[212:215], v[172:175]
	s_waitcnt lgkmcnt(4)
	v_mfma_f32_16x16x32_f16 v[82:85], v[82:85], v[216:219], v[94:97]
	s_waitcnt vmcnt(19)
	v_mfma_f32_16x16x32_f16 v[58:61], v[70:73], v[136:139], v[58:61]
	v_mfma_f32_16x16x32_f16 v[94:97], v[70:73], v[208:211], v[176:179]
	v_mfma_f32_16x16x32_f16 v[176:179], v[70:73], v[212:215], v[180:183]
	v_mfma_f32_16x16x32_f16 v[70:73], v[70:73], v[216:219], v[90:93]
	s_waitcnt vmcnt(18)
	v_mfma_f32_16x16x32_f16 v[54:57], v[62:65], v[136:139], v[54:57]
	v_mfma_f32_16x16x32_f16 v[90:93], v[62:65], v[208:211], v[184:187]
	v_mfma_f32_16x16x32_f16 v[180:183], v[62:65], v[212:215], v[188:191]
	v_mfma_f32_16x16x32_f16 v[62:65], v[62:65], v[216:219], v[78:81]
	s_waitcnt vmcnt(17)
	v_mfma_f32_16x16x32_f16 v[50:53], v[42:45], v[136:139], v[50:53]
	v_mfma_f32_16x16x32_f16 v[78:81], v[42:45], v[208:211], v[122:125]
	v_mfma_f32_16x16x32_f16 v[122:125], v[42:45], v[212:215], v[126:129]
	s_nop 2
	buffer_load_dwordx4 v[126:129], v147, s[16:19], s8 offen
	buffer_load_dwordx4 v[136:139], v148, s[16:19], s8 offen
	buffer_load_dwordx4 v[184:187], v149, s[16:19], s8 offen
	buffer_load_dwordx4 v[188:191], v150, s[16:19], s8 offen
	v_mfma_f32_16x16x32_f16 v[34:37], v[42:45], v[216:219], v[34:37]
	v_add_u32_e32 v111, s68, v111
	ds_read_b128 v[42:45], v111
	ds_read_b128 v[208:211], v111 offset:16384
	ds_read_b128 v[212:215], v111 offset:32768
	ds_read_b128 v[216:219], v111 offset:49152
	s_add_i32 s8, s22, s37
	s_waitcnt vmcnt(20) lgkmcnt(7)
	v_mfma_f32_16x16x32_f16 v[164:167], v[86:89], v[38:41], v[164:167]
	s_waitcnt lgkmcnt(6)
	v_mfma_f32_16x16x32_f16 v[168:171], v[86:89], v[156:159], v[168:171]
	s_waitcnt lgkmcnt(5)
	v_mfma_f32_16x16x32_f16 v[172:175], v[86:89], v[160:163], v[172:175]
	s_waitcnt lgkmcnt(4)
	v_mfma_f32_16x16x32_f16 v[82:85], v[86:89], v[228:231], v[82:85]
	s_waitcnt vmcnt(19)
	v_mfma_f32_16x16x32_f16 v[58:61], v[74:77], v[38:41], v[58:61]
	v_mfma_f32_16x16x32_f16 v[86:89], v[74:77], v[156:159], v[94:97]
	v_mfma_f32_16x16x32_f16 v[94:97], v[74:77], v[160:163], v[176:179]
	v_mfma_f32_16x16x32_f16 v[70:73], v[74:77], v[228:231], v[70:73]
	s_waitcnt vmcnt(18)
	v_mfma_f32_16x16x32_f16 v[54:57], v[66:69], v[38:41], v[54:57]
	v_mfma_f32_16x16x32_f16 v[74:77], v[66:69], v[156:159], v[90:93]
	v_mfma_f32_16x16x32_f16 v[90:93], v[66:69], v[160:163], v[180:183]
	v_mfma_f32_16x16x32_f16 v[62:65], v[66:69], v[228:231], v[62:65]
	s_waitcnt vmcnt(17)
	v_mfma_f32_16x16x32_f16 v[38:41], v[46:49], v[38:41], v[50:53]
	v_mfma_f32_16x16x32_f16 v[50:53], v[46:49], v[156:159], v[78:81]
	v_mfma_f32_16x16x32_f16 v[66:69], v[46:49], v[160:163], v[122:125]
	s_nop 1
	buffer_load_dwordx4 v[78:81], v147, s[16:19], s8 offen
	buffer_load_dwordx4 v[122:125], v148, s[16:19], s8 offen
	buffer_load_dwordx4 v[156:159], v149, s[16:19], s8 offen
	buffer_load_dwordx4 v[160:163], v150, s[16:19], s8 offen
	v_mfma_f32_16x16x32_f16 v[34:37], v[46:49], v[228:231], v[34:37]
	v_add_u32_e32 v98, s69, v98
	ds_read_b128 v[46:49], v98
	ds_read_b128 v[176:179], v98 offset:16384
	ds_read_b128 v[180:183], v98 offset:32768
	ds_read_b128 v[228:231], v98 offset:49152
	s_add_i32 s8, s22, s38
	s_waitcnt vmcnt(20) lgkmcnt(7)
	v_mfma_f32_16x16x32_f16 v[164:167], v[192:195], v[42:45], v[164:167]
	s_waitcnt lgkmcnt(6)
	v_mfma_f32_16x16x32_f16 v[168:171], v[192:195], v[208:211], v[168:171]
	s_waitcnt lgkmcnt(5)
	v_mfma_f32_16x16x32_f16 v[172:175], v[192:195], v[212:215], v[172:175]
	s_waitcnt lgkmcnt(4)
	v_mfma_f32_16x16x32_f16 v[82:85], v[192:195], v[216:219], v[82:85]
	s_waitcnt vmcnt(19)
	v_mfma_f32_16x16x32_f16 v[58:61], v[196:199], v[42:45], v[58:61]
	v_mfma_f32_16x16x32_f16 v[86:89], v[196:199], v[208:211], v[86:89]
	v_mfma_f32_16x16x32_f16 v[94:97], v[196:199], v[212:215], v[94:97]
	v_mfma_f32_16x16x32_f16 v[70:73], v[196:199], v[216:219], v[70:73]
	s_waitcnt vmcnt(18)
	v_mfma_f32_16x16x32_f16 v[54:57], v[200:203], v[42:45], v[54:57]
	v_mfma_f32_16x16x32_f16 v[74:77], v[200:203], v[208:211], v[74:77]
	v_mfma_f32_16x16x32_f16 v[90:93], v[200:203], v[212:215], v[90:93]
	v_mfma_f32_16x16x32_f16 v[62:65], v[200:203], v[216:219], v[62:65]
	s_waitcnt vmcnt(17)
	v_mfma_f32_16x16x32_f16 v[38:41], v[204:207], v[42:45], v[38:41]
	v_mfma_f32_16x16x32_f16 v[42:45], v[204:207], v[208:211], v[50:53]
	v_mfma_f32_16x16x32_f16 v[50:53], v[204:207], v[212:215], v[66:69]
	s_nop 2
	buffer_load_dwordx4 v[66:69], v147, s[16:19], s8 offen
	buffer_load_dwordx4 v[192:195], v148, s[16:19], s8 offen
	buffer_load_dwordx4 v[196:199], v149, s[16:19], s8 offen
	buffer_load_dwordx4 v[200:203], v150, s[16:19], s8 offen
	v_mfma_f32_16x16x32_f16 v[34:37], v[204:207], v[216:219], v[34:37]
	v_add_u32_e32 v99, s70, v99
	ds_read_b128 v[204:207], v99
	ds_read_b128 v[208:211], v99 offset:16384
	ds_read_b128 v[212:215], v99 offset:32768
	ds_read_b128 v[216:219], v99 offset:49152
	s_add_i32 s8, s22, s39
	s_waitcnt vmcnt(20) lgkmcnt(7)
	v_mfma_f32_16x16x32_f16 v[164:167], v[140:143], v[46:49], v[164:167]
	s_waitcnt lgkmcnt(6)
	v_mfma_f32_16x16x32_f16 v[168:171], v[140:143], v[176:179], v[168:171]
	s_waitcnt lgkmcnt(5)
	v_mfma_f32_16x16x32_f16 v[172:175], v[140:143], v[180:183], v[172:175]
	s_waitcnt lgkmcnt(4)
	v_mfma_f32_16x16x32_f16 v[82:85], v[140:143], v[228:231], v[82:85]
	s_waitcnt vmcnt(19)
	v_mfma_f32_16x16x32_f16 v[58:61], v[220:223], v[46:49], v[58:61]
	v_mfma_f32_16x16x32_f16 v[86:89], v[220:223], v[176:179], v[86:89]
	s_waitcnt vmcnt(18)
	v_mfma_f32_16x16x32_f16 v[54:57], v[152:155], v[46:49], v[54:57]
	v_mfma_f32_16x16x32_f16 v[74:77], v[152:155], v[176:179], v[74:77]
	v_mfma_f32_16x16x32_f16 v[90:93], v[152:155], v[180:183], v[90:93]
	v_mfma_f32_16x16x32_f16 v[62:65], v[152:155], v[228:231], v[62:65]
	s_waitcnt vmcnt(17)
	v_mfma_f32_16x16x32_f16 v[38:41], v[224:227], v[46:49], v[38:41]
	v_mfma_f32_16x16x32_f16 v[42:45], v[224:227], v[176:179], v[42:45]
	v_mfma_f32_16x16x32_f16 v[46:49], v[224:227], v[180:183], v[50:53]
	s_nop 2
	buffer_load_dwordx4 v[50:53], v147, s[16:19], s8 offen
	buffer_load_dwordx4 v[140:143], v148, s[16:19], s8 offen
	buffer_load_dwordx4 v[152:155], v149, s[16:19], s8 offen
	buffer_load_dwordx4 v[176:179], v150, s[16:19], s8 offen
	v_mfma_f32_16x16x32_f16 v[94:97], v[220:223], v[180:183], v[94:97]
	v_mfma_f32_16x16x32_f16 v[70:73], v[220:223], v[228:231], v[70:73]
	v_mfma_f32_16x16x32_f16 v[34:37], v[224:227], v[228:231], v[34:37]
	v_add_u32_e32 v100, s71, v100
	ds_read_b128 v[180:183], v100
	ds_read_b128 v[220:223], v100 offset:16384
	ds_read_b128 v[224:227], v100 offset:32768
	ds_read_b128 v[228:231], v100 offset:49152
	s_add_i32 s8, s22, s40
	s_waitcnt vmcnt(15) lgkmcnt(7)
	v_mfma_f32_16x16x32_f16 v[164:167], v[126:129], v[204:207], v[164:167]
	s_waitcnt lgkmcnt(6)
	v_mfma_f32_16x16x32_f16 v[168:171], v[126:129], v[208:211], v[168:171]
	s_waitcnt lgkmcnt(5)
	v_mfma_f32_16x16x32_f16 v[172:175], v[126:129], v[212:215], v[172:175]
	s_waitcnt lgkmcnt(4)
	v_mfma_f32_16x16x32_f16 v[82:85], v[126:129], v[216:219], v[82:85]
	s_waitcnt vmcnt(14)
	v_mfma_f32_16x16x32_f16 v[58:61], v[136:139], v[204:207], v[58:61]
	v_mfma_f32_16x16x32_f16 v[86:89], v[136:139], v[208:211], v[86:89]
	v_mfma_f32_16x16x32_f16 v[94:97], v[136:139], v[212:215], v[94:97]
	v_mfma_f32_16x16x32_f16 v[70:73], v[136:139], v[216:219], v[70:73]
	s_waitcnt vmcnt(13)
	v_mfma_f32_16x16x32_f16 v[54:57], v[184:187], v[204:207], v[54:57]
	v_mfma_f32_16x16x32_f16 v[74:77], v[184:187], v[208:211], v[74:77]
	v_mfma_f32_16x16x32_f16 v[90:93], v[184:187], v[212:215], v[90:93]
	v_mfma_f32_16x16x32_f16 v[62:65], v[184:187], v[216:219], v[62:65]
	s_waitcnt vmcnt(12)
	v_mfma_f32_16x16x32_f16 v[38:41], v[188:191], v[204:207], v[38:41]
	buffer_load_dwordx4 v[126:129], v147, s[16:19], s8 offen
	buffer_load_dwordx4 v[136:139], v148, s[16:19], s8 offen
	buffer_load_dwordx4 v[184:187], v149, s[16:19], s8 offen
	buffer_load_dwordx4 v[204:207], v150, s[16:19], s8 offen
	v_mfma_f32_16x16x32_f16 v[42:45], v[188:191], v[208:211], v[42:45]
	v_mfma_f32_16x16x32_f16 v[46:49], v[188:191], v[212:215], v[46:49]
	v_mfma_f32_16x16x32_f16 v[34:37], v[188:191], v[216:219], v[34:37]
	v_add_u32_e32 v111, s72, v111
	ds_read_b128 v[188:191], v111
	ds_read_b128 v[208:211], v111 offset:16384
	ds_read_b128 v[212:215], v111 offset:32768
	ds_read_b128 v[216:219], v111 offset:49152
	s_add_i32 s8, s22, s41
	s_waitcnt vmcnt(15) lgkmcnt(7)
	v_mfma_f32_16x16x32_f16 v[164:167], v[78:81], v[180:183], v[164:167]
	s_waitcnt lgkmcnt(6)
	v_mfma_f32_16x16x32_f16 v[168:171], v[78:81], v[220:223], v[168:171]
	s_waitcnt lgkmcnt(5)
	v_mfma_f32_16x16x32_f16 v[172:175], v[78:81], v[224:227], v[172:175]
	s_waitcnt lgkmcnt(4)
	v_mfma_f32_16x16x32_f16 v[78:81], v[78:81], v[228:231], v[82:85]
	s_waitcnt vmcnt(14)
	v_mfma_f32_16x16x32_f16 v[58:61], v[122:125], v[180:183], v[58:61]
	v_mfma_f32_16x16x32_f16 v[82:85], v[122:125], v[220:223], v[86:89]
	v_mfma_f32_16x16x32_f16 v[86:89], v[122:125], v[224:227], v[94:97]
	v_mfma_f32_16x16x32_f16 v[70:73], v[122:125], v[228:231], v[70:73]
	s_waitcnt vmcnt(13)
	v_mfma_f32_16x16x32_f16 v[54:57], v[156:159], v[180:183], v[54:57]
	v_mfma_f32_16x16x32_f16 v[74:77], v[156:159], v[220:223], v[74:77]
	v_mfma_f32_16x16x32_f16 v[90:93], v[156:159], v[224:227], v[90:93]
	v_mfma_f32_16x16x32_f16 v[62:65], v[156:159], v[228:231], v[62:65]
	s_waitcnt vmcnt(12)
	v_mfma_f32_16x16x32_f16 v[38:41], v[160:163], v[180:183], v[38:41]
	buffer_load_dwordx4 v[94:97], v147, s[16:19], s8 offen
	buffer_load_dwordx4 v[122:125], v148, s[16:19], s8 offen
	buffer_load_dwordx4 v[156:159], v149, s[16:19], s8 offen
	buffer_load_dwordx4 v[180:183], v150, s[16:19], s8 offen
	v_mfma_f32_16x16x32_f16 v[42:45], v[160:163], v[220:223], v[42:45]
	v_mfma_f32_16x16x32_f16 v[46:49], v[160:163], v[224:227], v[46:49]
	v_mfma_f32_16x16x32_f16 v[34:37], v[160:163], v[228:231], v[34:37]
	v_add_u32_e32 v98, s73, v98
	ds_read_b128 v[160:163], v98
	ds_read_b128 v[220:223], v98 offset:16384
	ds_read_b128 v[224:227], v98 offset:32768
	ds_read_b128 v[228:231], v98 offset:49152
	s_add_i32 s8, s22, s42
	s_waitcnt vmcnt(15) lgkmcnt(7)
	v_mfma_f32_16x16x32_f16 v[164:167], v[66:69], v[188:191], v[164:167]
	s_waitcnt lgkmcnt(6)
	v_mfma_f32_16x16x32_f16 v[168:171], v[66:69], v[208:211], v[168:171]
	s_waitcnt lgkmcnt(5)
	v_mfma_f32_16x16x32_f16 v[172:175], v[66:69], v[212:215], v[172:175]
	s_waitcnt lgkmcnt(4)
	v_mfma_f32_16x16x32_f16 v[66:69], v[66:69], v[216:219], v[78:81]
	s_waitcnt vmcnt(14)
	v_mfma_f32_16x16x32_f16 v[58:61], v[192:195], v[188:191], v[58:61]
	v_mfma_f32_16x16x32_f16 v[78:81], v[192:195], v[208:211], v[82:85]
	v_mfma_f32_16x16x32_f16 v[82:85], v[192:195], v[212:215], v[86:89]
	v_mfma_f32_16x16x32_f16 v[70:73], v[192:195], v[216:219], v[70:73]
	s_waitcnt vmcnt(13)
	v_mfma_f32_16x16x32_f16 v[54:57], v[196:199], v[188:191], v[54:57]
	v_mfma_f32_16x16x32_f16 v[74:77], v[196:199], v[208:211], v[74:77]
	v_mfma_f32_16x16x32_f16 v[86:89], v[196:199], v[212:215], v[90:93]
	v_mfma_f32_16x16x32_f16 v[62:65], v[196:199], v[216:219], v[62:65]
	s_waitcnt vmcnt(12)
	v_mfma_f32_16x16x32_f16 v[38:41], v[200:203], v[188:191], v[38:41]
	buffer_load_dwordx4 v[90:93], v147, s[16:19], s8 offen
	buffer_load_dwordx4 v[188:191], v148, s[16:19], s8 offen
	buffer_load_dwordx4 v[192:195], v149, s[16:19], s8 offen
	buffer_load_dwordx4 v[196:199], v150, s[16:19], s8 offen
	v_mfma_f32_16x16x32_f16 v[42:45], v[200:203], v[208:211], v[42:45]
	v_mfma_f32_16x16x32_f16 v[46:49], v[200:203], v[212:215], v[46:49]
	v_mfma_f32_16x16x32_f16 v[34:37], v[200:203], v[216:219], v[34:37]
	v_add_u32_e32 v99, s74, v99
	ds_read_b128 v[200:203], v99
	ds_read_b128 v[208:211], v99 offset:16384
	ds_read_b128 v[212:215], v99 offset:32768
	ds_read_b128 v[216:219], v99 offset:49152
	s_add_i32 s8, s22, s43
	s_waitcnt vmcnt(15) lgkmcnt(7)
	v_mfma_f32_16x16x32_f16 v[164:167], v[50:53], v[160:163], v[164:167]
	s_waitcnt lgkmcnt(6)
	v_mfma_f32_16x16x32_f16 v[168:171], v[50:53], v[220:223], v[168:171]
	s_waitcnt lgkmcnt(5)
	v_mfma_f32_16x16x32_f16 v[172:175], v[50:53], v[224:227], v[172:175]
	s_waitcnt lgkmcnt(4)
	v_mfma_f32_16x16x32_f16 v[50:53], v[50:53], v[228:231], v[66:69]
	s_waitcnt vmcnt(14)
	v_mfma_f32_16x16x32_f16 v[58:61], v[140:143], v[160:163], v[58:61]
	v_mfma_f32_16x16x32_f16 v[66:69], v[140:143], v[220:223], v[78:81]
	v_mfma_f32_16x16x32_f16 v[78:81], v[140:143], v[224:227], v[82:85]
	v_mfma_f32_16x16x32_f16 v[70:73], v[140:143], v[228:231], v[70:73]
	s_waitcnt vmcnt(13)
	v_mfma_f32_16x16x32_f16 v[54:57], v[152:155], v[160:163], v[54:57]
	v_mfma_f32_16x16x32_f16 v[74:77], v[152:155], v[220:223], v[74:77]
	v_mfma_f32_16x16x32_f16 v[82:85], v[152:155], v[224:227], v[86:89]
	v_mfma_f32_16x16x32_f16 v[62:65], v[152:155], v[228:231], v[62:65]
	s_waitcnt vmcnt(12)
	v_mfma_f32_16x16x32_f16 v[38:41], v[176:179], v[160:163], v[38:41]
	buffer_load_dwordx4 v[86:89], v147, s[16:19], s8 offen
	buffer_load_dwordx4 v[140:143], v148, s[16:19], s8 offen
	buffer_load_dwordx4 v[152:155], v149, s[16:19], s8 offen
	buffer_load_dwordx4 v[160:163], v150, s[16:19], s8 offen
	v_mfma_f32_16x16x32_f16 v[42:45], v[176:179], v[220:223], v[42:45]
	v_mfma_f32_16x16x32_f16 v[46:49], v[176:179], v[224:227], v[46:49]
	v_mfma_f32_16x16x32_f16 v[34:37], v[176:179], v[228:231], v[34:37]
	v_add_u32_e32 v100, s75, v100
	ds_read_b128 v[176:179], v100
	ds_read_b128 v[220:223], v100 offset:16384
	ds_read_b128 v[224:227], v100 offset:32768
	ds_read_b128 v[228:231], v100 offset:49152
	s_add_i32 s8, s22, s44
	s_waitcnt vmcnt(15) lgkmcnt(7)
	v_mfma_f32_16x16x32_f16 v[164:167], v[126:129], v[200:203], v[164:167]
	s_waitcnt lgkmcnt(6)
	v_mfma_f32_16x16x32_f16 v[168:171], v[126:129], v[208:211], v[168:171]
	s_waitcnt lgkmcnt(5)
	v_mfma_f32_16x16x32_f16 v[172:175], v[126:129], v[212:215], v[172:175]
	s_waitcnt lgkmcnt(4)
	v_mfma_f32_16x16x32_f16 v[50:53], v[126:129], v[216:219], v[50:53]
	s_waitcnt vmcnt(14)
	v_mfma_f32_16x16x32_f16 v[58:61], v[136:139], v[200:203], v[58:61]
	v_mfma_f32_16x16x32_f16 v[66:69], v[136:139], v[208:211], v[66:69]
	v_mfma_f32_16x16x32_f16 v[78:81], v[136:139], v[212:215], v[78:81]
	v_mfma_f32_16x16x32_f16 v[70:73], v[136:139], v[216:219], v[70:73]
	s_waitcnt vmcnt(13)
	v_mfma_f32_16x16x32_f16 v[54:57], v[184:187], v[200:203], v[54:57]
	v_mfma_f32_16x16x32_f16 v[74:77], v[184:187], v[208:211], v[74:77]
	v_mfma_f32_16x16x32_f16 v[82:85], v[184:187], v[212:215], v[82:85]
	v_mfma_f32_16x16x32_f16 v[62:65], v[184:187], v[216:219], v[62:65]
	s_waitcnt vmcnt(12)
	v_mfma_f32_16x16x32_f16 v[38:41], v[204:207], v[200:203], v[38:41]
	buffer_load_dwordx4 v[126:129], v147, s[16:19], s8 offen
	buffer_load_dwordx4 v[136:139], v148, s[16:19], s8 offen
	buffer_load_dwordx4 v[184:187], v149, s[16:19], s8 offen
	buffer_load_dwordx4 v[200:203], v150, s[16:19], s8 offen
	v_mfma_f32_16x16x32_f16 v[42:45], v[204:207], v[208:211], v[42:45]
	v_mfma_f32_16x16x32_f16 v[46:49], v[204:207], v[212:215], v[46:49]
	v_mfma_f32_16x16x32_f16 v[34:37], v[204:207], v[216:219], v[34:37]
	v_add_u32_e32 v111, s76, v111
	ds_read_b128 v[204:207], v111
	ds_read_b128 v[208:211], v111 offset:16384
	ds_read_b128 v[212:215], v111 offset:32768
	ds_read_b128 v[216:219], v111 offset:49152
	s_add_i32 s8, s22, s45
	s_waitcnt vmcnt(15) lgkmcnt(7)
	v_mfma_f32_16x16x32_f16 v[164:167], v[94:97], v[176:179], v[164:167]
	s_waitcnt lgkmcnt(6)
	v_mfma_f32_16x16x32_f16 v[168:171], v[94:97], v[220:223], v[168:171]
	s_waitcnt vmcnt(14)
	v_mfma_f32_16x16x32_f16 v[58:61], v[122:125], v[176:179], v[58:61]
	v_mfma_f32_16x16x32_f16 v[66:69], v[122:125], v[220:223], v[66:69]
	s_waitcnt lgkmcnt(5)
	v_mfma_f32_16x16x32_f16 v[78:81], v[122:125], v[224:227], v[78:81]
	s_waitcnt lgkmcnt(4)
	v_mfma_f32_16x16x32_f16 v[70:73], v[122:125], v[228:231], v[70:73]
	s_waitcnt vmcnt(13)
	v_mfma_f32_16x16x32_f16 v[54:57], v[156:159], v[176:179], v[54:57]
	v_mfma_f32_16x16x32_f16 v[74:77], v[156:159], v[220:223], v[74:77]
	v_mfma_f32_16x16x32_f16 v[82:85], v[156:159], v[224:227], v[82:85]
	v_mfma_f32_16x16x32_f16 v[62:65], v[156:159], v[228:231], v[62:65]
	s_waitcnt vmcnt(12)
	v_mfma_f32_16x16x32_f16 v[38:41], v[180:183], v[176:179], v[38:41]
	v_mfma_f32_16x16x32_f16 v[42:45], v[180:183], v[220:223], v[42:45]
	buffer_load_dwordx4 v[122:125], v147, s[16:19], s8 offen
	buffer_load_dwordx4 v[156:159], v148, s[16:19], s8 offen
	buffer_load_dwordx4 v[176:179], v149, s[16:19], s8 offen
	buffer_load_dwordx4 v[220:223], v150, s[16:19], s8 offen
	v_mfma_f32_16x16x32_f16 v[50:53], v[94:97], v[228:231], v[50:53]
	v_mfma_f32_16x16x32_f16 v[46:49], v[180:183], v[224:227], v[46:49]
	v_mfma_f32_16x16x32_f16 v[34:37], v[180:183], v[228:231], v[34:37]
	v_mfma_f32_16x16x32_f16 v[172:175], v[94:97], v[224:227], v[172:175]
	v_add_u32_e32 v98, s77, v98
	ds_read_b128 v[94:97], v98
	ds_read_b128 v[180:183], v98 offset:16384
	ds_read_b128 v[224:227], v98 offset:32768
	ds_read_b128 v[228:231], v98 offset:49152
	s_add_i32 s8, s22, s46
	s_waitcnt vmcnt(15) lgkmcnt(7)
	v_mfma_f32_16x16x32_f16 v[164:167], v[90:93], v[204:207], v[164:167]
	s_waitcnt lgkmcnt(6)
	v_mfma_f32_16x16x32_f16 v[168:171], v[90:93], v[208:211], v[168:171]
	s_waitcnt lgkmcnt(5)
	v_mfma_f32_16x16x32_f16 v[172:175], v[90:93], v[212:215], v[172:175]
	s_waitcnt lgkmcnt(4)
	v_mfma_f32_16x16x32_f16 v[90:93], v[90:93], v[216:219], v[50:53]
	s_waitcnt vmcnt(14)
	v_mfma_f32_16x16x32_f16 v[232:235], v[188:191], v[204:207], v[58:61]
	v_mfma_f32_16x16x32_f16 v[66:69], v[188:191], v[208:211], v[66:69]
	v_mfma_f32_16x16x32_f16 v[78:81], v[188:191], v[212:215], v[78:81]
	v_mfma_f32_16x16x32_f16 v[70:73], v[188:191], v[216:219], v[70:73]
	s_waitcnt vmcnt(13)
	v_mfma_f32_16x16x32_f16 v[188:191], v[192:195], v[204:207], v[54:57]
	v_mfma_f32_16x16x32_f16 v[74:77], v[192:195], v[208:211], v[74:77]
	v_mfma_f32_16x16x32_f16 v[82:85], v[192:195], v[212:215], v[82:85]
	v_mfma_f32_16x16x32_f16 v[62:65], v[192:195], v[216:219], v[62:65]
	s_waitcnt vmcnt(12)
	v_mfma_f32_16x16x32_f16 v[192:195], v[196:199], v[204:207], v[38:41]
	buffer_load_dwordx4 v[58:61], v147, s[16:19], s8 offen
	buffer_load_dwordx4 v[54:57], v148, s[16:19], s8 offen
	buffer_load_dwordx4 v[50:53], v149, s[16:19], s8 offen
	buffer_load_dwordx4 v[38:41], v150, s[16:19], s8 offen
	v_mfma_f32_16x16x32_f16 v[42:45], v[196:199], v[208:211], v[42:45]
	v_mfma_f32_16x16x32_f16 v[46:49], v[196:199], v[212:215], v[46:49]
	v_mfma_f32_16x16x32_f16 v[196:199], v[196:199], v[216:219], v[34:37]
	v_add_u32_e32 v99, s78, v99
	ds_read_b128 v[204:207], v99
	ds_read_b128 v[208:211], v99 offset:16384
	ds_read_b128 v[212:215], v99 offset:32768
	ds_read_b128 v[216:219], v99 offset:49152
	s_add_i32 s8, s22, s47
	s_waitcnt vmcnt(15) lgkmcnt(7)
	v_mfma_f32_16x16x32_f16 v[164:167], v[86:89], v[94:97], v[164:167]
	s_waitcnt lgkmcnt(6)
	v_mfma_f32_16x16x32_f16 v[168:171], v[86:89], v[180:183], v[168:171]
	s_waitcnt lgkmcnt(5)
	v_mfma_f32_16x16x32_f16 v[172:175], v[86:89], v[224:227], v[172:175]
	s_waitcnt lgkmcnt(4)
	v_mfma_f32_16x16x32_f16 v[86:89], v[86:89], v[228:231], v[90:93]
	s_waitcnt vmcnt(14)
	v_mfma_f32_16x16x32_f16 v[232:235], v[140:143], v[94:97], v[232:235]
	v_mfma_f32_16x16x32_f16 v[66:69], v[140:143], v[180:183], v[66:69]
	v_mfma_f32_16x16x32_f16 v[236:239], v[140:143], v[224:227], v[78:81]
	v_mfma_f32_16x16x32_f16 v[70:73], v[140:143], v[228:231], v[70:73]
	s_waitcnt vmcnt(13)
	v_mfma_f32_16x16x32_f16 v[140:143], v[152:155], v[94:97], v[188:191]
	v_mfma_f32_16x16x32_f16 v[74:77], v[152:155], v[180:183], v[74:77]
	v_mfma_f32_16x16x32_f16 v[82:85], v[152:155], v[224:227], v[82:85]
	v_mfma_f32_16x16x32_f16 v[62:65], v[152:155], v[228:231], v[62:65]
	s_waitcnt vmcnt(12)
	v_mfma_f32_16x16x32_f16 v[152:155], v[160:163], v[94:97], v[192:195]
	buffer_load_dwordx4 v[94:97], v147, s[16:19], s8 offen
	buffer_load_dwordx4 v[90:93], v148, s[16:19], s8 offen
	buffer_load_dwordx4 v[78:81], v149, s[16:19], s8 offen
	buffer_load_dwordx4 v[34:37], v150, s[16:19], s8 offen
	v_mfma_f32_16x16x32_f16 v[42:45], v[160:163], v[180:183], v[42:45]
	v_mfma_f32_16x16x32_f16 v[46:49], v[160:163], v[224:227], v[46:49]
	v_mfma_f32_16x16x32_f16 v[160:163], v[160:163], v[228:231], v[196:199]
	v_add_u32_e32 v100, s79, v100
	ds_read_b128 v[180:183], v100
	ds_read_b128 v[188:191], v100 offset:16384
	ds_read_b128 v[192:195], v100 offset:32768
	ds_read_b128 v[196:199], v100 offset:49152
	s_add_i32 s8, s22, s48
	s_waitcnt vmcnt(15) lgkmcnt(7)
	v_mfma_f32_16x16x32_f16 v[164:167], v[126:129], v[204:207], v[164:167]
	s_waitcnt lgkmcnt(6)
	v_mfma_f32_16x16x32_f16 v[168:171], v[126:129], v[208:211], v[168:171]
	s_waitcnt lgkmcnt(5)
	v_mfma_f32_16x16x32_f16 v[172:175], v[126:129], v[212:215], v[172:175]
	s_waitcnt lgkmcnt(4)
	v_mfma_f32_16x16x32_f16 v[86:89], v[126:129], v[216:219], v[86:89]
	s_waitcnt vmcnt(14)
	v_mfma_f32_16x16x32_f16 v[126:129], v[136:139], v[204:207], v[232:235]
	v_mfma_f32_16x16x32_f16 v[66:69], v[136:139], v[208:211], v[66:69]
	v_mfma_f32_16x16x32_f16 v[224:227], v[136:139], v[212:215], v[236:239]
	v_mfma_f32_16x16x32_f16 v[136:139], v[136:139], v[216:219], v[70:73]
	s_waitcnt vmcnt(13)
	v_mfma_f32_16x16x32_f16 v[140:143], v[184:187], v[204:207], v[140:143]
	v_mfma_f32_16x16x32_f16 v[74:77], v[184:187], v[208:211], v[74:77]
	v_mfma_f32_16x16x32_f16 v[228:231], v[184:187], v[212:215], v[82:85]
	v_mfma_f32_16x16x32_f16 v[184:187], v[184:187], v[216:219], v[62:65]
	s_waitcnt vmcnt(12)
	v_mfma_f32_16x16x32_f16 v[152:155], v[200:203], v[204:207], v[152:155]
	v_mfma_f32_16x16x32_f16 v[204:207], v[200:203], v[208:211], v[42:45]
	buffer_load_dwordx4 v[82:85], v147, s[16:19], s8 offen
	buffer_load_dwordx4 v[70:73], v148, s[16:19], s8 offen
	buffer_load_dwordx4 v[62:65], v149, s[16:19], s8 offen
	buffer_load_dwordx4 v[42:45], v150, s[16:19], s8 offen
	v_mfma_f32_16x16x32_f16 v[46:49], v[200:203], v[212:215], v[46:49]
	v_mfma_f32_16x16x32_f16 v[160:163], v[200:203], v[216:219], v[160:163]
	v_add_u32_e32 v0, 0x1ac00, v104
	ds_read_b128 v[240:243], v0
	ds_read_b128 v[244:247], v0 offset:16
	s_waitcnt vmcnt(12) lgkmcnt(5)
	v_mfma_f32_16x16x32_f16 v[164:167], v[122:125], v[180:183], v[164:167]
	v_mfma_f32_16x16x32_f16 v[126:129], v[156:159], v[180:183], v[126:129]
	v_mfma_f32_16x16x32_f16 v[140:143], v[176:179], v[180:183], v[140:143]
	v_mfma_f32_16x16x32_f16 v[152:155], v[220:223], v[180:183], v[152:155]
	s_waitcnt lgkmcnt(4)
	v_mfma_f32_16x16x32_f16 v[168:171], v[122:125], v[188:191], v[168:171]
	v_mfma_f32_16x16x32_f16 v[208:211], v[156:159], v[188:191], v[66:69]
	v_mfma_f32_16x16x32_f16 v[212:215], v[176:179], v[188:191], v[74:77]
	v_mfma_f32_16x16x32_f16 v[204:207], v[220:223], v[188:191], v[204:207]
	s_waitcnt lgkmcnt(3)
	v_mfma_f32_16x16x32_f16 v[172:175], v[122:125], v[192:195], v[172:175]
	v_cvt_pk_f16_f32 v232, v164, v165
	v_cvt_pk_f16_f32 v233, v166, v167
	v_pk_max_f16 v232, v232, 0
	v_pk_max_f16 v233, v233, 0
	v_mfma_f32_16x16x32_f16 v[224:227], v[156:159], v[192:195], v[224:227]
	v_cvt_pk_f16_f32 v234, v126, v127
	v_cvt_pk_f16_f32 v235, v128, v129
	v_pk_max_f16 v234, v234, 0
	v_pk_max_f16 v235, v235, 0
	v_mfma_f32_16x16x32_f16 v[228:231], v[176:179], v[192:195], v[228:231]
	v_cvt_pk_f16_f32 v236, v140, v141
	v_cvt_pk_f16_f32 v237, v142, v143
	v_pk_max_f16 v236, v236, 0
	v_pk_max_f16 v237, v237, 0
	v_mfma_f32_16x16x32_f16 v[216:219], v[220:223], v[192:195], v[46:49]
	v_cvt_pk_f16_f32 v238, v152, v153
	v_cvt_pk_f16_f32 v239, v154, v155
	v_pk_max_f16 v238, v238, 0
	v_pk_max_f16 v239, v239, 0
	s_waitcnt lgkmcnt(2)
	v_mfma_f32_16x16x32_f16 v[200:203], v[122:125], v[196:199], v[86:89]
	v_cvt_pk_f16_f32 v180, v168, v169
	v_cvt_pk_f16_f32 v181, v170, v171
	v_pk_max_f16 v180, v180, 0
	v_pk_max_f16 v181, v181, 0
	s_add_i32 s8, s22, s49
	buffer_load_dwordx4 v[86:89], v147, s[16:19], s8 offen
	buffer_load_dwordx4 v[74:77], v148, s[16:19], s8 offen
	buffer_load_dwordx4 v[66:69], v149, s[16:19], s8 offen
	buffer_load_dwordx4 v[46:49], v150, s[16:19], s8 offen
	v_mfma_f32_16x16x32_f16 v[136:139], v[156:159], v[196:199], v[136:139]
	v_cvt_pk_f16_f32 v182, v208, v209
	v_cvt_pk_f16_f32 v183, v210, v211
	v_pk_max_f16 v182, v182, 0
	v_pk_max_f16 v183, v183, 0
	s_waitcnt lgkmcnt(1)
	v_mfma_f32_16x16x32_f16 v[252:255], v[240:243], v[232:235], 0
	v_cvt_pk_f16_f32 v232, v172, v173
	v_cvt_pk_f16_f32 v233, v174, v175
	v_pk_max_f16 v232, v232, 0
	v_pk_max_f16 v233, v233, 0
	v_mfma_f32_16x16x32_f16 v[184:187], v[176:179], v[196:199], v[184:187]
	v_cvt_pk_f16_f32 v188, v212, v213
	v_cvt_pk_f16_f32 v189, v214, v215
	v_pk_max_f16 v188, v188, 0
	v_pk_max_f16 v189, v189, 0
	s_waitcnt lgkmcnt(0)
	v_mfma_f32_16x16x32_f16 v[252:255], v[244:247], v[236:239], v[252:255]
	ds_read_u16 v102, v114
	ds_read_u16 v103, v114 offset:512
	ds_read_u16 v115, v114 offset:1024
	ds_read_u16 v116, v114 offset:1536
	v_cvt_pk_f16_f32 v234, v224, v225
	v_cvt_pk_f16_f32 v235, v226, v227
	v_pk_max_f16 v234, v234, 0
	v_pk_max_f16 v235, v235, 0
	v_mfma_f32_16x16x32_f16 v[160:163], v[220:223], v[196:199], v[160:163]
	v_cvt_pk_f16_f32 v190, v204, v205
	v_cvt_pk_f16_f32 v191, v206, v207
	v_pk_max_f16 v190, v190, 0
	v_pk_max_f16 v191, v191, 0
	v_mfma_f32_16x16x32_f16 v[192:195], v[240:243], v[180:183], 0
	v_cvt_pk_f16_f32 v236, v228, v229
	v_cvt_pk_f16_f32 v237, v230, v231
	v_pk_max_f16 v236, v236, 0
	v_pk_max_f16 v237, v237, 0
	v_mfma_f32_16x16x32_f16 v[192:195], v[244:247], v[188:191], v[192:195]
	v_cvt_pk_f16_f32 v238, v216, v217
	v_cvt_pk_f16_f32 v239, v218, v219
	v_pk_max_f16 v238, v238, 0
	v_pk_max_f16 v239, v239, 0
	v_cvt_pk_f16_f32 v180, v200, v201
	v_cvt_pk_f16_f32 v181, v202, v203
	v_pk_max_f16 v180, v180, 0
	v_pk_max_f16 v181, v181, 0
	v_mfma_f32_16x16x32_f16 v[196:199], v[240:243], v[232:235], 0
	v_cvt_pk_f16_f32 v182, v136, v137
	v_cvt_pk_f16_f32 v183, v138, v139
	v_pk_max_f16 v182, v182, 0
	v_pk_max_f16 v183, v183, 0
	v_mfma_f32_16x16x32_f16 v[196:199], v[244:247], v[236:239], v[196:199]
	v_cvt_pk_f16_f32 v188, v184, v185
	v_cvt_pk_f16_f32 v189, v186, v187
	v_pk_max_f16 v188, v188, 0
	v_pk_max_f16 v189, v189, 0
	v_cvt_pk_f16_f32 v190, v160, v161
	v_cvt_pk_f16_f32 v191, v162, v163
	v_pk_max_f16 v190, v190, 0
	v_pk_max_f16 v191, v191, 0
	v_mfma_f32_16x16x32_f16 v[122:125], v[240:243], v[180:183], 0
	s_nop 0
	v_mfma_f32_16x16x32_f16 v[122:125], v[244:247], v[188:191], v[122:125]
	v_add_u32_e32 v145, 0x12c00, v105
	ds_read_b128 v[240:243], v145 offset:2048
	ds_read_b128 v[244:247], v145 offset:2064
	ds_read_b128 v[248:251], v145 offset:2080
	s_load_dword s30, s[12:13], 0x0
	v_cndmask_b32_e64 v0, v252, v192, s[2:3]
	ds_read_b128 v[252:255], v145 offset:2096
	v_cndmask_b32_e64 v0, v0, v196, s[0:1]
	v_cndmask_b32_e64 v0, v0, v122, s[26:27]
	ds_write_b32 v112, v0
	s_waitcnt vmcnt(16)
	v_cndmask_b32_e64 v1, v30, v134, s[0:1]
	v_bfi_b32 v30, s10, v1, v30
	v_perm_b32 v1, v22, v134, s24
	v_cndmask_b32_e64 v22, v22, v1, s[0:1]
	v_bfi_b32 v1, s10, v135, v18
	v_perm_b32 v121, v10, v135, s24
	v_cndmask_b32_e64 v18, v18, v1, s[0:1]
	v_cndmask_b32_e64 v10, v10, v121, s[0:1]
	s_add_i32 s22, s22, 0x80000
	s_add_i32 s11, s11, 1
	s_add_u32 s12, s12, 4
	s_addc_u32 s13, s13, 0
	v_add_u32_e32 v104, 0x400, v104
	v_add_u32_e32 v105, 0x800, v105
	v_add_u32_e32 v114, 2, v114
	s_cmp_eq_u32 s22, 0x898000
	s_waitcnt lgkmcnt(0)
	s_barrier
	ds_read_b128 v[232:235], v113
	ds_read_b128 v[236:239], v113 offset:1024
	s_waitcnt lgkmcnt(0)
	v_add_f32_e32 v0, v232, v233
	v_add_f32_e32 v1, v234, v235
	v_add_f32_e32 v121, v236, v237
	v_add_f32_e32 v144, v238, v239
	v_add_f32_e32 v0, v0, v1
	v_add_f32_e32 v121, v121, v144
	v_add_f32_e32 v0, v0, v121
	v_add_f32_e32 v0, s30, v0
	ds_write_b32 v106, v0
	v_cvt_f16_f32_e32 v1, v0
	v_cvt_f16_f32_e32 v121, v0
	s_nop 1
	v_permlane16_swap_b32_e32 v1, v121
	v_mov_b32_e32 v144, v1
	v_mov_b32_e32 v145, v121
	s_nop 1
	v_permlane32_swap_b32_e32 v1, v144
	v_permlane32_swap_b32_e32 v121, v145
	v_add_u32_e32 v106, 4, v106
	s_cbranch_scc0 .LBB1_4
